# v72 plus sel-attn quad-tiles keep -mrun*log2e (and mrun+6 for quad 0) in registers, updated only in the rescale branch
# speedup vs baseline: 1.0110x; 1.0014x over previous
;     ...
;         float mrun[NQ], lrun[NQ]; f32x4 O[NQ][4];
; #pragma unroll
;         for (int qd = 0; qd < NQ; ++qd) { mrun[qd] = -1e30f; lrun[qd] = 0.f;
; #pragma unroll
;             for (int dt = 0; dt < 4; ++dt) O[qd][dt] = (f32x4){0.f, 0.f, 0.f, 0.f}; }
;         float carry3[NQ]; for (int i = 0; i < NQ; ++i) carry3[i] = 0.f;
;         const int npass = (MODE == 2) ? ((DBG == 6) ? 1 : (DBG == 7 ? 0 : 2)) : 1;
;         for (int pass = 0; pass < npass; ++pass) {
;             const bool do_pv = (MODE != 2) || pass == 1;
;             float linv[NQ];
;             if (MODE == 2 && pass == 1) {
; #pragma unroll
;                 for (int qd = 0; qd < NQ; ++qd) { float mt = mrun[qd]; mt = fmaxf(mt, __shfl_xor(mt, 16)); mt = fmaxf(mt, __shfl_xor(mt, 32));
;                     float lt = lrun[qd] * __expf(mrun[qd] - mt); lt += __shfl_xor(lt, 16); lt += __shfl_xor(lt, 32); mrun[qd] = mt; linv[qd] = lt > 0.f ? -__builtin_amdgcn_logf(lt) : 0.f; }
;             }
;     ...
;             const unsigned kthr = (unsigned)(c.tid >> 3) * (unsigned)kstride + (unsigned)(c.tid & 7) * 8u, vthr = (unsigned)(c.tid >> 3) * (unsigned)vstride + (unsigned)(c.tid & 7) * 8u;
;             int st_k, st_va;
;             { const int row = c.tid >> 3, cj = c.tid & 7, ga = 2 * cj;
;               st_k = row * 128 + (((cj ^ row) & 7) << 4);
;               st_va = row * 128 + (((((ga >> 3) * 4 + (ga & 3)) ^ row) & 7) << 4) + ((ga >> 2) & 1) * 8; }
;             u32x4 kreg[TS], vreg[TS]; int p0n[TS];
;             const int nrounds = (ntiles + TS - 1) / TS;
.LBB0_1149:
	s_or_b64 exec, exec, s[2:3]
	s_andn2_b64 vcc, exec, s[0:1]
	s_cbranch_vccnz .LBB0_1309
	s_add_i32 s0, s13, 6
	s_mul_hi_i32 s1, s0, 0x92492493
	s_add_i32 s1, s1, s0
	s_lshr_b32 s0, s1, 31
	s_ashr_i32 s14, s1, 2
	v_mov_b32_e32 v86, v1
	v_mov_b32_e32 v87, v1
	v_mov_b32_e32 v88, v1
	v_mov_b32_e32 v89, v1
	s_add_i32 s14, s14, s0
	v_mov_b32_e32 v203, 0
	v_mov_b64_e32 v[92:93], v[88:89]
	v_mov_b64_e32 v[96:97], v[88:89]
	v_mov_b64_e32 v[100:101], v[88:89]
	v_mov_b64_e32 v[104:105], v[88:89]
	v_mov_b64_e32 v[82:83], v[86:87]
	v_mov_b64_e32 v[78:79], v[86:87]
	v_mov_b64_e32 v[74:75], v[86:87]
	s_or_b32 s15, s22, 7
	s_sub_i32 s16, s22, 63
	s_max_i32 s17, s14, 1
	s_mov_b32 s54, 0
	v_mov_b32_e32 v167, 0xf149f2ca
	v_mov_b32_e32 v186, 0
	v_mov_b32_e32 v188, 0xf149f2ca
	v_mov_b32_e32 v250, 0
	s_mov_b32 s55, 13
	v_mov_b64_e32 v[90:91], v[86:87]
	v_mov_b64_e32 v[94:95], v[86:87]
	v_mov_b64_e32 v[98:99], v[86:87]
	v_mov_b64_e32 v[102:103], v[86:87]
	v_mov_b64_e32 v[84:85], v[88:89]
	v_mov_b64_e32 v[80:81], v[88:89]
	v_mov_b64_e32 v[76:77], v[88:89]
	v_mov_b32_e32 v202, v203
	v_mov_b32_e32 v236, 0xf149f2ca
	s_mov_b32 s62, s29
	s_mov_b32 s61, s53
	s_mov_b32 s60, s63
	s_mov_b32 s59, s64
	s_mov_b32 s58, s65
	s_mov_b32 s57, s66
	s_mov_b32 s56, s67

; __device__ __forceinline__ float dpp_xor1(float v) { return __int_as_float(__builtin_amdgcn_update_dpp(0, __float_as_int(v), 0xB1, 0xf, 0xf, false)); }
;     ...
;                             if (__any(mx > mrun[qd] + 6.0f)) {
;                                 mx = fmaxf(mx, __shfl_xor(mx, 16)); mx = fmaxf(mx, __shfl_xor(mx, 32));
;                                 const float mn = fmaxf(mrun[qd], mx), corr = __expf(mrun[qd] - mn); mrun[qd] = mn;
;                                 lrun[qd] *= corr;
; #pragma unroll
;                                 for (int dt = 0; dt < 4; ++dt) O[qd][dt] = O[qd][dt] * corr;
;                             }
;                             float negm = (mrun[qd] < -1e29f ? 0.f : -mrun[qd] * L2E) + boff; float ps = 0.f;
;                             if (MODE == 3 && !colsel) negm = -__builtin_inff();
; #pragma unroll
;                             for (int kt = 0; kt < 4; ++kt)
; #pragma unroll
;                                 for (int r = 0; r < 4; ++r) { p[kt][r] = (DBG == 2) ? sc[kt][r] + negm : __builtin_amdgcn_exp2f(__builtin_fmaf(sc[kt][r], L2E, negm)); ps += p[kt][r]; }
;                             lrun[qd] += ps;
;                         }
;                         if (MODE == 2 && pass == 1) {
;                             float base[4], im3[4], rot[4];
; #pragma unroll
;                             for (int kt = 0; kt < 4; ++kt) { float im[4];
; #pragma unroll
;                                 for (int r = 0; r < 4; ++r) { float v = p[kt][r]; v += dpp_xor1(v); v += dpp_xor2(v); im[r] = v; }
;                                 base[kt] = 2.0f * (im[0] + im[1] + im[2]) + im[3]; im3[kt] = im[3]; }
; #pragma unroll
;                             for (int kt = 0; kt < 4; ++kt) rot[kt] = __shfl(im3[kt], (lane + 48) & 63);
; #pragma unroll
;                             for (int kt = 0; kt < 4; ++kt) { const float pv3 = q > 0 ? rot[kt] : (kt == 0 ? carry3[qd] : rot[kt > 0 ? kt - 1 : 0]);
;                                 const int jg = (p0 + 16 * kt + 4 * q) >> 2;
;                                 if (hr == 0 && jg < 256) sscore[(tq - t0) * SSTR + jg] = base[kt] + pv3; }
;                             carry3[qd] = rot[3];
;                         }
;                         if (do_pv && DBG != 1) {
; #pragma unroll
;                             for (int st = 0; st < 2; ++st) {
.LBB0_1163:
	v_and_b32_e32 v192, s0, v191
	v_cmp_eq_u32_e64 s[4:5], 0, v192
	v_max3_f32 v192, v150, v151, v152
	v_max3_f32 v192, v192, v153, v146
	v_max3_f32 v192, v192, v147, v148
	v_max3_f32 v192, v192, v149, v142
	v_max3_f32 v192, v192, v143, v144
	v_max3_f32 v192, v192, v145, v110
	v_max3_f32 v192, v192, v111, v112
	v_max_f32_e32 v192, v192, v113
	v_add_f32_e32 v192, v237, v192
	v_cndmask_b32_e64 v192, v192, v190, s[4:5]
	v_cmp_gt_f32_e32 vcc, v192, v188
	s_cbranch_vccz .LBB0_1165
	ds_bpermute_b32 v193, v230, v192
	v_max_f32_e32 v192, v192, v192
	s_waitcnt lgkmcnt(0)
	v_max_f32_e32 v193, v193, v193
	v_max_f32_e32 v192, v192, v193
	ds_bpermute_b32 v193, v231, v192
	s_waitcnt lgkmcnt(0)
	v_max3_f32 v193, v167, v192, v193
	v_sub_f32_e32 v167, v167, v193
	v_mul_f32_e32 v167, 0x3fb8aa3b, v167
	v_exp_f32_e32 v192, v167
	v_mov_b32_e32 v167, v193
	v_mul_f32_e32 v203, v203, v192
	v_pk_mul_f32 v[104:105], v[104:105], v[192:193] op_sel_hi:[1,0]
	v_pk_mul_f32 v[102:103], v[102:103], v[192:193] op_sel_hi:[1,0]
	v_pk_mul_f32 v[100:101], v[100:101], v[192:193] op_sel_hi:[1,0]
	v_pk_mul_f32 v[98:99], v[98:99], v[192:193] op_sel_hi:[1,0]
	v_pk_mul_f32 v[96:97], v[96:97], v[192:193] op_sel_hi:[1,0]
	v_pk_mul_f32 v[94:95], v[94:95], v[192:193] op_sel_hi:[1,0]
	v_pk_mul_f32 v[92:93], v[92:93], v[192:193] op_sel_hi:[1,0]
	v_pk_mul_f32 v[90:91], v[90:91], v[192:193] op_sel_hi:[1,0]
	v_add_f32_e32 v188, 0x40c00000, v193
	v_mul_f32_e32 v186, 0xbfb8aa3b, v193
	v_cmp_ngt_f32_e32 vcc, s30, v193
	s_nop 1
	v_cndmask_b32_e32 v186, 0, v186, vcc
.LBB0_1165:
	v_fmamk_f32 v192, v237, 0x3fb8aa3b, v186
	v_cndmask_b32_e64 v192, v192, v194, s[4:5]
	v_fmamk_f32 v150, v150, 0x3fb8aa3b, v192
	v_fmamk_f32 v151, v151, 0x3fb8aa3b, v192
	v_fmamk_f32 v152, v152, 0x3fb8aa3b, v192
	v_fmamk_f32 v153, v153, 0x3fb8aa3b, v192
	v_fmamk_f32 v146, v146, 0x3fb8aa3b, v192
	v_fmamk_f32 v147, v147, 0x3fb8aa3b, v192
	v_fmamk_f32 v148, v148, 0x3fb8aa3b, v192
	v_fmamk_f32 v149, v149, 0x3fb8aa3b, v192
	v_exp_f32_e32 v150, v150
	v_exp_f32_e32 v151, v151
	v_exp_f32_e32 v152, v152
	v_exp_f32_e32 v153, v153
	v_exp_f32_e32 v146, v146
	v_exp_f32_e32 v147, v147
	v_exp_f32_e32 v148, v148
	v_exp_f32_e32 v149, v149
	v_fmamk_f32 v142, v142, 0x3fb8aa3b, v192
	v_exp_f32_e32 v237, v142
	v_fmamk_f32 v142, v143, 0x3fb8aa3b, v192
	v_exp_f32_e32 v238, v142
	v_fmamk_f32 v142, v144, 0x3fb8aa3b, v192
	v_add_f32_e32 v193, 0, v150
	v_exp_f32_e32 v239, v142
	v_fmamk_f32 v240, v145, 0x3fb8aa3b, v192
	v_cvt_pk_bf16_f32 v142, v150, v151
	v_cvt_pk_bf16_f32 v143, v152, v153
	v_cvt_pk_bf16_f32 v144, v146, v147
	v_cvt_pk_bf16_f32 v145, v148, v149
	v_fmamk_f32 v110, v110, 0x3fb8aa3b, v192
	v_add_f32_e32 v193, v151, v193
	s_waitcnt lgkmcnt(7)
	v_mfma_f32_16x16x32_bf16 v[102:105], v[138:141], v[142:145], v[102:105]
	v_exp_f32_e32 v139, v110
	v_fmamk_f32 v110, v111, 0x3fb8aa3b, v192
	v_add_f32_e32 v193, v152, v193
	s_waitcnt lgkmcnt(6)
	v_mfma_f32_16x16x32_bf16 v[98:101], v[134:137], v[142:145], v[98:101]
	v_exp_f32_e32 v134, v110
	v_fmamk_f32 v110, v112, 0x3fb8aa3b, v192
	v_fmac_f32_e32 v192, 0x3fb8aa3b, v113
	v_add_f32_e32 v193, v153, v193
	v_exp_f32_e32 v138, v240
	s_waitcnt lgkmcnt(5)
	v_mfma_f32_16x16x32_bf16 v[94:97], v[130:133], v[142:145], v[94:97]
	v_exp_f32_e32 v130, v110
	v_exp_f32_e32 v131, v192
	v_add_f32_e32 v193, v146, v193
	v_add_f32_e32 v193, v147, v193
	v_add_f32_e32 v193, v148, v193
	v_add_f32_e32 v193, v149, v193
	v_cvt_pk_bf16_f32 v110, v237, v238
	v_cvt_pk_bf16_f32 v111, v239, v138
	v_cvt_pk_bf16_f32 v112, v139, v134
	v_cvt_pk_bf16_f32 v113, v130, v131
	s_waitcnt lgkmcnt(4)
	v_mfma_f32_16x16x32_bf16 v[90:93], v[126:129], v[142:145], v[90:93]
	s_waitcnt lgkmcnt(3)
	v_mfma_f32_16x16x32_bf16 v[102:105], v[122:125], v[110:113], v[102:105]
	v_add_f32_e32 v122, v237, v193
	v_add_f32_e32 v122, v238, v122
	v_add_f32_e32 v122, v239, v122
	s_waitcnt lgkmcnt(2)
	v_mfma_f32_16x16x32_bf16 v[98:101], v[118:121], v[110:113], v[98:101]
	v_add_f32_e32 v118, v138, v122
	v_add_f32_e32 v118, v139, v118
	v_add_f32_e32 v118, v134, v118
	s_waitcnt lgkmcnt(1)
	v_mfma_f32_16x16x32_bf16 v[94:97], v[114:117], v[110:113], v[94:97]
	v_add_f32_e32 v114, v130, v118
	v_add_f32_e32 v114, v131, v114
	v_add_f32_e32 v203, v203, v114
	s_waitcnt lgkmcnt(0)
	v_mfma_f32_16x16x32_bf16 v[90:93], v[106:109], v[110:113], v[90:93]

; __device__ __forceinline__ float dpp_xor1(float v) { return __int_as_float(__builtin_amdgcn_update_dpp(0, __float_as_int(v), 0xB1, 0xf, 0xf, false)); }
;     ...
;                             if (__any(mx > mrun[qd] + 6.0f)) {
;                                 mx = fmaxf(mx, __shfl_xor(mx, 16)); mx = fmaxf(mx, __shfl_xor(mx, 32));
;                                 const float mn = fmaxf(mrun[qd], mx), corr = __expf(mrun[qd] - mn); mrun[qd] = mn;
;                                 lrun[qd] *= corr;
; #pragma unroll
;                                 for (int dt = 0; dt < 4; ++dt) O[qd][dt] = O[qd][dt] * corr;
;                             }
;                             float negm = (mrun[qd] < -1e29f ? 0.f : -mrun[qd] * L2E) + boff; float ps = 0.f;
;                             if (MODE == 3 && !colsel) negm = -__builtin_inff();
; #pragma unroll
;                             for (int kt = 0; kt < 4; ++kt)
; #pragma unroll
;                                 for (int r = 0; r < 4; ++r) { p[kt][r] = (DBG == 2) ? sc[kt][r] + negm : __builtin_amdgcn_exp2f(__builtin_fmaf(sc[kt][r], L2E, negm)); ps += p[kt][r]; }
;                             lrun[qd] += ps;
;                         }
;                         if (MODE == 2 && pass == 1) {
;                             float base[4], im3[4], rot[4];
; #pragma unroll
;                             for (int kt = 0; kt < 4; ++kt) { float im[4];
; #pragma unroll
;                                 for (int r = 0; r < 4; ++r) { float v = p[kt][r]; v += dpp_xor1(v); v += dpp_xor2(v); im[r] = v; }
;                                 base[kt] = 2.0f * (im[0] + im[1] + im[2]) + im[3]; im3[kt] = im[3]; }
; #pragma unroll
;                             for (int kt = 0; kt < 4; ++kt) rot[kt] = __shfl(im3[kt], (lane + 48) & 63);
; #pragma unroll
;                             for (int kt = 0; kt < 4; ++kt) { const float pv3 = q > 0 ? rot[kt] : (kt == 0 ? carry3[qd] : rot[kt > 0 ? kt - 1 : 0]);
;                                 const int jg = (p0 + 16 * kt + 4 * q) >> 2;
;                                 if (hr == 0 && jg < 256) sscore[(tq - t0) * SSTR + jg] = base[kt] + pv3; }
;                             carry3[qd] = rot[3];
;                         }
;                         if (do_pv && DBG != 1) {
; #pragma unroll
;                             for (int st = 0; st < 2; ++st) {
.LBB0_1172:
	v_and_b32_e32 v192, s0, v205
	v_cmp_eq_u32_e64 s[0:1], 0, v192
	v_max3_f32 v192, v150, v151, v152
	v_max3_f32 v192, v192, v153, v146
	v_max3_f32 v192, v192, v147, v148
	v_max3_f32 v192, v192, v149, v142
	v_max3_f32 v192, v192, v143, v144
	v_max3_f32 v192, v192, v145, v110
	v_max3_f32 v192, v192, v111, v112
	v_max_f32_e32 v192, v192, v113
	v_add_f32_e32 v192, v237, v192
	v_cndmask_b32_e64 v192, v192, v190, s[0:1]
	v_add_f32_e32 v193, 0x40c00000, v236
	v_cmp_gt_f32_e32 vcc, v192, v193
	s_cbranch_vccz .LBB0_1174
	ds_bpermute_b32 v193, v230, v192
	v_max_f32_e32 v192, v192, v192
	s_waitcnt lgkmcnt(0)
	v_max_f32_e32 v193, v193, v193
	v_max_f32_e32 v192, v192, v193
	ds_bpermute_b32 v193, v231, v192
	s_waitcnt lgkmcnt(0)
	v_max3_f32 v193, v236, v192, v193
	v_sub_f32_e32 v192, v236, v193
	v_mul_f32_e32 v192, 0x3fb8aa3b, v192
	v_exp_f32_e32 v192, v192
	v_mov_b32_e32 v236, v193
	v_mul_f32_e32 v202, v202, v192
	v_pk_mul_f32 v[88:89], v[88:89], v[192:193] op_sel_hi:[1,0]
	v_pk_mul_f32 v[86:87], v[86:87], v[192:193] op_sel_hi:[1,0]
	v_pk_mul_f32 v[84:85], v[84:85], v[192:193] op_sel_hi:[1,0]
	v_pk_mul_f32 v[82:83], v[82:83], v[192:193] op_sel_hi:[1,0]
	v_pk_mul_f32 v[80:81], v[80:81], v[192:193] op_sel_hi:[1,0]
	v_pk_mul_f32 v[78:79], v[78:79], v[192:193] op_sel_hi:[1,0]
	v_pk_mul_f32 v[76:77], v[76:77], v[192:193] op_sel_hi:[1,0]
	v_pk_mul_f32 v[74:75], v[74:75], v[192:193] op_sel_hi:[1,0]
	v_mul_f32_e32 v250, 0xbfb8aa3b, v193
	v_cmp_ngt_f32_e32 vcc, s30, v193
	s_nop 1
	v_cndmask_b32_e32 v250, 0, v250, vcc
.LBB0_1174:
	v_fmamk_f32 v192, v237, 0x3fb8aa3b, v250
	v_cndmask_b32_e64 v192, v192, v194, s[0:1]
	v_fmamk_f32 v150, v150, 0x3fb8aa3b, v192
	v_fmamk_f32 v151, v151, 0x3fb8aa3b, v192
	v_fmamk_f32 v152, v152, 0x3fb8aa3b, v192
	v_fmamk_f32 v153, v153, 0x3fb8aa3b, v192
	v_fmamk_f32 v146, v146, 0x3fb8aa3b, v192
	v_fmamk_f32 v147, v147, 0x3fb8aa3b, v192
	v_fmamk_f32 v148, v148, 0x3fb8aa3b, v192
	v_fmamk_f32 v149, v149, 0x3fb8aa3b, v192
	v_exp_f32_e32 v150, v150
	v_exp_f32_e32 v151, v151
	v_exp_f32_e32 v152, v152
	v_exp_f32_e32 v153, v153
	v_exp_f32_e32 v146, v146
	v_exp_f32_e32 v147, v147
	v_exp_f32_e32 v148, v148
	v_exp_f32_e32 v149, v149
	v_fmamk_f32 v142, v142, 0x3fb8aa3b, v192
	v_exp_f32_e32 v237, v142
	v_fmamk_f32 v142, v143, 0x3fb8aa3b, v192
	v_exp_f32_e32 v238, v142
	v_fmamk_f32 v142, v144, 0x3fb8aa3b, v192
	v_add_f32_e32 v193, 0, v150
	v_exp_f32_e32 v239, v142
	v_fmamk_f32 v240, v145, 0x3fb8aa3b, v192
	v_cvt_pk_bf16_f32 v142, v150, v151
	v_cvt_pk_bf16_f32 v143, v152, v153
	v_cvt_pk_bf16_f32 v144, v146, v147
	v_cvt_pk_bf16_f32 v145, v148, v149
	v_fmamk_f32 v110, v110, 0x3fb8aa3b, v192
	v_add_f32_e32 v193, v151, v193
	s_waitcnt lgkmcnt(7)
	v_mfma_f32_16x16x32_bf16 v[86:89], v[138:141], v[142:145], v[86:89]
	v_exp_f32_e32 v139, v110
	v_fmamk_f32 v110, v111, 0x3fb8aa3b, v192
	v_add_f32_e32 v193, v152, v193
	s_waitcnt lgkmcnt(6)
	v_mfma_f32_16x16x32_bf16 v[82:85], v[134:137], v[142:145], v[82:85]
	v_exp_f32_e32 v134, v110
	v_fmamk_f32 v110, v112, 0x3fb8aa3b, v192
	v_fmac_f32_e32 v192, 0x3fb8aa3b, v113
	v_add_f32_e32 v193, v153, v193
	v_exp_f32_e32 v138, v240
	s_waitcnt lgkmcnt(5)
	v_mfma_f32_16x16x32_bf16 v[78:81], v[130:133], v[142:145], v[78:81]
	v_exp_f32_e32 v130, v110
	v_exp_f32_e32 v131, v192
	v_add_f32_e32 v193, v146, v193
	v_add_f32_e32 v193, v147, v193
	v_add_f32_e32 v193, v148, v193
	v_add_f32_e32 v193, v149, v193
	v_cvt_pk_bf16_f32 v110, v237, v238
	v_cvt_pk_bf16_f32 v111, v239, v138
	v_cvt_pk_bf16_f32 v112, v139, v134
	v_cvt_pk_bf16_f32 v113, v130, v131
	s_waitcnt lgkmcnt(4)
	v_mfma_f32_16x16x32_bf16 v[74:77], v[126:129], v[142:145], v[74:77]
	s_waitcnt lgkmcnt(3)
	v_mfma_f32_16x16x32_bf16 v[86:89], v[122:125], v[110:113], v[86:89]
	v_add_f32_e32 v122, v237, v193
	v_add_f32_e32 v122, v238, v122
	v_add_f32_e32 v122, v239, v122
	s_waitcnt lgkmcnt(2)
	v_mfma_f32_16x16x32_bf16 v[82:85], v[118:121], v[110:113], v[82:85]
	v_add_f32_e32 v118, v138, v122
	v_add_f32_e32 v118, v139, v118
	v_add_f32_e32 v118, v134, v118
	s_waitcnt lgkmcnt(1)
	v_mfma_f32_16x16x32_bf16 v[78:81], v[114:117], v[110:113], v[78:81]
	v_add_f32_e32 v114, v130, v118
	v_add_f32_e32 v114, v131, v114
	v_add_f32_e32 v202, v202, v114
	s_waitcnt lgkmcnt(0)
	v_mfma_f32_16x16x32_bf16 v[74:77], v[106:109], v[110:113], v[74:77]

; __device__ __forceinline__ float dpp_xor1(float v) { return __int_as_float(__builtin_amdgcn_update_dpp(0, __float_as_int(v), 0xB1, 0xf, 0xf, false)); }
;     ...
;                             if (__any(mx > mrun[qd] + 6.0f)) {
;                                 mx = fmaxf(mx, __shfl_xor(mx, 16)); mx = fmaxf(mx, __shfl_xor(mx, 32));
;                                 const float mn = fmaxf(mrun[qd], mx), corr = __expf(mrun[qd] - mn); mrun[qd] = mn;
;                                 lrun[qd] *= corr;
; #pragma unroll
;                                 for (int dt = 0; dt < 4; ++dt) O[qd][dt] = O[qd][dt] * corr;
;                             }
;                             float negm = (mrun[qd] < -1e29f ? 0.f : -mrun[qd] * L2E) + boff; float ps = 0.f;
;                             if (MODE == 3 && !colsel) negm = -__builtin_inff();
; #pragma unroll
;                             for (int kt = 0; kt < 4; ++kt)
; #pragma unroll
;                                 for (int r = 0; r < 4; ++r) { p[kt][r] = (DBG == 2) ? sc[kt][r] + negm : __builtin_amdgcn_exp2f(__builtin_fmaf(sc[kt][r], L2E, negm)); ps += p[kt][r]; }
;                             lrun[qd] += ps;
;                         }
;                         if (MODE == 2 && pass == 1) {
;                             float base[4], im3[4], rot[4];
; #pragma unroll
;                             for (int kt = 0; kt < 4; ++kt) { float im[4];
; #pragma unroll
;                                 for (int r = 0; r < 4; ++r) { float v = p[kt][r]; v += dpp_xor1(v); v += dpp_xor2(v); im[r] = v; }
;                                 base[kt] = 2.0f * (im[0] + im[1] + im[2]) + im[3]; im3[kt] = im[3]; }
; #pragma unroll
;                             for (int kt = 0; kt < 4; ++kt) rot[kt] = __shfl(im3[kt], (lane + 48) & 63);
; #pragma unroll
;                             for (int kt = 0; kt < 4; ++kt) { const float pv3 = q > 0 ? rot[kt] : (kt == 0 ? carry3[qd] : rot[kt > 0 ? kt - 1 : 0]);
;                                 const int jg = (p0 + 16 * kt + 4 * q) >> 2;
;                                 if (hr == 0 && jg < 256) sscore[(tq - t0) * SSTR + jg] = base[kt] + pv3; }
;                             carry3[qd] = rot[3];
;                         }
;                         if (do_pv && DBG != 1) {
; #pragma unroll
;                             for (int st = 0; st < 2; ++st) {
.LBB0_1229:
	v_and_b32_e32 v192, s0, v191
	v_cmp_eq_u32_e64 s[4:5], 0, v192
	v_max3_f32 v192, v150, v151, v152
	v_max3_f32 v192, v192, v153, v146
	v_max3_f32 v192, v192, v147, v148
	v_max3_f32 v192, v192, v149, v142
	v_max3_f32 v192, v192, v143, v144
	v_max3_f32 v192, v192, v145, v110
	v_max3_f32 v192, v192, v111, v112
	v_max_f32_e32 v192, v192, v113
	v_add_f32_e32 v192, v239, v192
	v_cndmask_b32_e64 v192, v192, v190, s[4:5]
	v_cmp_gt_f32_e32 vcc, v192, v188
	s_cbranch_vccz .LBB0_1231
	ds_bpermute_b32 v193, v230, v192
	v_max_f32_e32 v192, v192, v192
	s_waitcnt lgkmcnt(0)
	v_max_f32_e32 v193, v193, v193
	v_max_f32_e32 v192, v192, v193
	ds_bpermute_b32 v193, v231, v192
	s_waitcnt lgkmcnt(0)
	v_max3_f32 v193, v167, v192, v193
	v_sub_f32_e32 v167, v167, v193
	v_mul_f32_e32 v167, 0x3fb8aa3b, v167
	v_exp_f32_e32 v192, v167
	v_mov_b32_e32 v167, v193
	v_mul_f32_e32 v203, v203, v192
	v_pk_mul_f32 v[104:105], v[104:105], v[192:193] op_sel_hi:[1,0]
	v_pk_mul_f32 v[102:103], v[102:103], v[192:193] op_sel_hi:[1,0]
	v_pk_mul_f32 v[100:101], v[100:101], v[192:193] op_sel_hi:[1,0]
	v_pk_mul_f32 v[98:99], v[98:99], v[192:193] op_sel_hi:[1,0]
	v_pk_mul_f32 v[96:97], v[96:97], v[192:193] op_sel_hi:[1,0]
	v_pk_mul_f32 v[94:95], v[94:95], v[192:193] op_sel_hi:[1,0]
	v_pk_mul_f32 v[92:93], v[92:93], v[192:193] op_sel_hi:[1,0]
	v_pk_mul_f32 v[90:91], v[90:91], v[192:193] op_sel_hi:[1,0]
	v_add_f32_e32 v188, 0x40c00000, v193
	v_mul_f32_e32 v186, 0xbfb8aa3b, v193
	v_cmp_ngt_f32_e32 vcc, s30, v193
	s_nop 1
	v_cndmask_b32_e32 v186, 0, v186, vcc
.LBB0_1231:
	v_fmamk_f32 v192, v239, 0x3fb8aa3b, v186
	v_cndmask_b32_e64 v192, v192, v194, s[4:5]
	v_fmamk_f32 v150, v150, 0x3fb8aa3b, v192
	v_fmamk_f32 v151, v151, 0x3fb8aa3b, v192
	v_fmamk_f32 v152, v152, 0x3fb8aa3b, v192
	v_fmamk_f32 v153, v153, 0x3fb8aa3b, v192
	v_fmamk_f32 v146, v146, 0x3fb8aa3b, v192
	v_fmamk_f32 v147, v147, 0x3fb8aa3b, v192
	v_fmamk_f32 v148, v148, 0x3fb8aa3b, v192
	v_fmamk_f32 v149, v149, 0x3fb8aa3b, v192
	v_exp_f32_e32 v150, v150
	v_exp_f32_e32 v151, v151
	v_exp_f32_e32 v152, v152
	v_exp_f32_e32 v153, v153
	v_exp_f32_e32 v146, v146
	v_exp_f32_e32 v147, v147
	v_exp_f32_e32 v148, v148
	v_exp_f32_e32 v149, v149
	v_fmamk_f32 v142, v142, 0x3fb8aa3b, v192
	v_exp_f32_e32 v239, v142
	v_fmamk_f32 v142, v143, 0x3fb8aa3b, v192
	v_exp_f32_e32 v240, v142
	v_fmamk_f32 v142, v144, 0x3fb8aa3b, v192
	v_add_f32_e32 v193, 0, v150
	v_exp_f32_e32 v241, v142
	v_fmamk_f32 v242, v145, 0x3fb8aa3b, v192
	v_cvt_pk_bf16_f32 v142, v150, v151
	v_cvt_pk_bf16_f32 v143, v152, v153
	v_cvt_pk_bf16_f32 v144, v146, v147
	v_cvt_pk_bf16_f32 v145, v148, v149
	v_fmamk_f32 v110, v110, 0x3fb8aa3b, v192
	v_add_f32_e32 v193, v151, v193
	s_waitcnt lgkmcnt(7)
	v_mfma_f32_16x16x32_bf16 v[102:105], v[138:141], v[142:145], v[102:105]
	v_exp_f32_e32 v139, v110
	v_fmamk_f32 v110, v111, 0x3fb8aa3b, v192
	v_add_f32_e32 v193, v152, v193
	s_waitcnt lgkmcnt(6)
	v_mfma_f32_16x16x32_bf16 v[98:101], v[134:137], v[142:145], v[98:101]
	v_exp_f32_e32 v134, v110
	v_fmamk_f32 v110, v112, 0x3fb8aa3b, v192
	v_fmac_f32_e32 v192, 0x3fb8aa3b, v113
	v_add_f32_e32 v193, v153, v193
	v_exp_f32_e32 v138, v242
	s_waitcnt lgkmcnt(5)
	v_mfma_f32_16x16x32_bf16 v[94:97], v[130:133], v[142:145], v[94:97]
	v_exp_f32_e32 v130, v110
	v_exp_f32_e32 v131, v192
	v_add_f32_e32 v193, v146, v193
	v_add_f32_e32 v193, v147, v193
	v_add_f32_e32 v193, v148, v193
	v_add_f32_e32 v193, v149, v193
	v_cvt_pk_bf16_f32 v110, v239, v240
	v_cvt_pk_bf16_f32 v111, v241, v138
	v_cvt_pk_bf16_f32 v112, v139, v134
	v_cvt_pk_bf16_f32 v113, v130, v131
	s_waitcnt lgkmcnt(4)
	v_mfma_f32_16x16x32_bf16 v[90:93], v[126:129], v[142:145], v[90:93]
	s_waitcnt lgkmcnt(3)
	v_mfma_f32_16x16x32_bf16 v[102:105], v[122:125], v[110:113], v[102:105]
	v_add_f32_e32 v122, v239, v193
	v_add_f32_e32 v122, v240, v122
	v_add_f32_e32 v122, v241, v122
	s_waitcnt lgkmcnt(2)
	v_mfma_f32_16x16x32_bf16 v[98:101], v[118:121], v[110:113], v[98:101]
	v_add_f32_e32 v118, v138, v122
	v_add_f32_e32 v118, v139, v118
	v_add_f32_e32 v118, v134, v118
	s_waitcnt lgkmcnt(1)
	v_mfma_f32_16x16x32_bf16 v[94:97], v[114:117], v[110:113], v[94:97]
	v_add_f32_e32 v114, v130, v118
	v_add_f32_e32 v114, v131, v114
	v_add_f32_e32 v203, v203, v114
	s_waitcnt lgkmcnt(0)
	v_mfma_f32_16x16x32_bf16 v[90:93], v[106:109], v[110:113], v[90:93]

; __device__ __forceinline__ float dpp_xor1(float v) { return __int_as_float(__builtin_amdgcn_update_dpp(0, __float_as_int(v), 0xB1, 0xf, 0xf, false)); }
;     ...
;                             if (__any(mx > mrun[qd] + 6.0f)) {
;                                 mx = fmaxf(mx, __shfl_xor(mx, 16)); mx = fmaxf(mx, __shfl_xor(mx, 32));
;                                 const float mn = fmaxf(mrun[qd], mx), corr = __expf(mrun[qd] - mn); mrun[qd] = mn;
;                                 lrun[qd] *= corr;
; #pragma unroll
;                                 for (int dt = 0; dt < 4; ++dt) O[qd][dt] = O[qd][dt] * corr;
;                             }
;                             float negm = (mrun[qd] < -1e29f ? 0.f : -mrun[qd] * L2E) + boff; float ps = 0.f;
;                             if (MODE == 3 && !colsel) negm = -__builtin_inff();
; #pragma unroll
;                             for (int kt = 0; kt < 4; ++kt)
; #pragma unroll
;                                 for (int r = 0; r < 4; ++r) { p[kt][r] = (DBG == 2) ? sc[kt][r] + negm : __builtin_amdgcn_exp2f(__builtin_fmaf(sc[kt][r], L2E, negm)); ps += p[kt][r]; }
;                             lrun[qd] += ps;
;                         }
;                         if (MODE == 2 && pass == 1) {
;                             float base[4], im3[4], rot[4];
; #pragma unroll
;                             for (int kt = 0; kt < 4; ++kt) { float im[4];
; #pragma unroll
;                                 for (int r = 0; r < 4; ++r) { float v = p[kt][r]; v += dpp_xor1(v); v += dpp_xor2(v); im[r] = v; }
;                                 base[kt] = 2.0f * (im[0] + im[1] + im[2]) + im[3]; im3[kt] = im[3]; }
; #pragma unroll
;                             for (int kt = 0; kt < 4; ++kt) rot[kt] = __shfl(im3[kt], (lane + 48) & 63);
; #pragma unroll
;                             for (int kt = 0; kt < 4; ++kt) { const float pv3 = q > 0 ? rot[kt] : (kt == 0 ? carry3[qd] : rot[kt > 0 ? kt - 1 : 0]);
;                                 const int jg = (p0 + 16 * kt + 4 * q) >> 2;
;                                 if (hr == 0 && jg < 256) sscore[(tq - t0) * SSTR + jg] = base[kt] + pv3; }
;                             carry3[qd] = rot[3];
;                         }
;                         if (do_pv && DBG != 1) {
; #pragma unroll
;                             for (int st = 0; st < 2; ++st) {
.LBB0_1251:
	v_and_b32_e32 v192, s0, v191
	v_cmp_eq_u32_e64 s[4:5], 0, v192
	v_max3_f32 v192, v150, v151, v152
	v_max3_f32 v192, v192, v153, v146
	v_max3_f32 v192, v192, v147, v148
	v_max3_f32 v192, v192, v149, v142
	v_max3_f32 v192, v192, v143, v144
	v_max3_f32 v192, v192, v145, v106
	v_max3_f32 v192, v192, v107, v108
	v_max_f32_e32 v192, v192, v109
	v_add_f32_e32 v192, v248, v192
	v_cndmask_b32_e64 v192, v192, v190, s[4:5]
	v_cmp_gt_f32_e32 vcc, v192, v188
	s_cbranch_vccz .LBB0_1253
	ds_bpermute_b32 v193, v230, v192
	v_max_f32_e32 v192, v192, v192
	s_waitcnt lgkmcnt(0)
	v_max_f32_e32 v193, v193, v193
	v_max_f32_e32 v192, v192, v193
	ds_bpermute_b32 v193, v231, v192
	s_waitcnt lgkmcnt(0)
	v_max3_f32 v193, v167, v192, v193
	v_sub_f32_e32 v167, v167, v193
	v_mul_f32_e32 v167, 0x3fb8aa3b, v167
	v_exp_f32_e32 v192, v167
	v_mov_b32_e32 v167, v193
	v_mul_f32_e32 v203, v203, v192
	v_pk_mul_f32 v[104:105], v[104:105], v[192:193] op_sel_hi:[1,0]
	v_pk_mul_f32 v[102:103], v[102:103], v[192:193] op_sel_hi:[1,0]
	v_pk_mul_f32 v[100:101], v[100:101], v[192:193] op_sel_hi:[1,0]
	v_pk_mul_f32 v[98:99], v[98:99], v[192:193] op_sel_hi:[1,0]
	v_pk_mul_f32 v[96:97], v[96:97], v[192:193] op_sel_hi:[1,0]
	v_pk_mul_f32 v[94:95], v[94:95], v[192:193] op_sel_hi:[1,0]
	v_pk_mul_f32 v[92:93], v[92:93], v[192:193] op_sel_hi:[1,0]
	v_pk_mul_f32 v[90:91], v[90:91], v[192:193] op_sel_hi:[1,0]
	v_add_f32_e32 v188, 0x40c00000, v193
	v_mul_f32_e32 v186, 0xbfb8aa3b, v193
	v_cmp_ngt_f32_e32 vcc, s30, v193
	s_nop 1
	v_cndmask_b32_e32 v186, 0, v186, vcc
.LBB0_1253:
	v_fmamk_f32 v192, v248, 0x3fb8aa3b, v186
	v_cndmask_b32_e64 v192, v192, v194, s[4:5]
	v_fmamk_f32 v150, v150, 0x3fb8aa3b, v192
	v_fmamk_f32 v151, v151, 0x3fb8aa3b, v192
	v_fmamk_f32 v152, v152, 0x3fb8aa3b, v192
	v_fmamk_f32 v153, v153, 0x3fb8aa3b, v192
	v_fmamk_f32 v146, v146, 0x3fb8aa3b, v192
	v_fmamk_f32 v147, v147, 0x3fb8aa3b, v192
	v_fmamk_f32 v148, v148, 0x3fb8aa3b, v192
	v_fmamk_f32 v149, v149, 0x3fb8aa3b, v192
	v_exp_f32_e32 v150, v150
	v_exp_f32_e32 v151, v151
	v_exp_f32_e32 v152, v152
	v_exp_f32_e32 v153, v153
	v_exp_f32_e32 v146, v146
	v_exp_f32_e32 v147, v147
	v_exp_f32_e32 v148, v148
	v_exp_f32_e32 v149, v149
	v_fmamk_f32 v142, v142, 0x3fb8aa3b, v192
	v_exp_f32_e32 v242, v142
	v_fmamk_f32 v142, v143, 0x3fb8aa3b, v192
	v_exp_f32_e32 v243, v142
	v_fmamk_f32 v142, v144, 0x3fb8aa3b, v192
	v_add_f32_e32 v193, 0, v150
	v_exp_f32_e32 v248, v142
	v_fmamk_f32 v249, v145, 0x3fb8aa3b, v192
	v_cvt_pk_bf16_f32 v142, v150, v151
	v_cvt_pk_bf16_f32 v143, v152, v153
	v_cvt_pk_bf16_f32 v144, v146, v147
	v_cvt_pk_bf16_f32 v145, v148, v149
	v_fmamk_f32 v106, v106, 0x3fb8aa3b, v192
	v_add_f32_e32 v193, v151, v193
	s_waitcnt lgkmcnt(7)
	v_mfma_f32_16x16x32_bf16 v[102:105], v[138:141], v[142:145], v[102:105]
	v_exp_f32_e32 v139, v106
	v_fmamk_f32 v106, v107, 0x3fb8aa3b, v192
	v_add_f32_e32 v193, v152, v193
	s_waitcnt lgkmcnt(6)
	v_mfma_f32_16x16x32_bf16 v[98:101], v[130:133], v[142:145], v[98:101]
	v_exp_f32_e32 v130, v106
	v_fmamk_f32 v106, v108, 0x3fb8aa3b, v192
	v_fmac_f32_e32 v192, 0x3fb8aa3b, v109
	v_add_f32_e32 v193, v153, v193
	v_exp_f32_e32 v138, v249
	v_exp_f32_e32 v131, v106
	v_exp_f32_e32 v132, v192
	v_add_f32_e32 v193, v146, v193
	v_add_f32_e32 v193, v147, v193
	v_add_f32_e32 v193, v148, v193
	v_add_f32_e32 v193, v149, v193
	v_cvt_pk_bf16_f32 v106, v242, v243
	v_cvt_pk_bf16_f32 v107, v248, v138
	v_cvt_pk_bf16_f32 v108, v139, v130
	v_cvt_pk_bf16_f32 v109, v131, v132
	s_waitcnt lgkmcnt(5)
	v_mfma_f32_16x16x32_bf16 v[94:97], v[134:137], v[142:145], v[94:97]
	s_waitcnt lgkmcnt(3)
	v_mfma_f32_16x16x32_bf16 v[102:105], v[122:125], v[106:109], v[102:105]
	v_add_f32_e32 v122, v242, v193
	v_add_f32_e32 v122, v243, v122
	v_add_f32_e32 v122, v248, v122
	v_mfma_f32_16x16x32_bf16 v[90:93], v[126:129], v[142:145], v[90:93]
	s_waitcnt lgkmcnt(2)
	v_mfma_f32_16x16x32_bf16 v[98:101], v[118:121], v[106:109], v[98:101]
	v_add_f32_e32 v118, v138, v122
	v_add_f32_e32 v118, v139, v118
	v_add_f32_e32 v118, v130, v118
	s_waitcnt lgkmcnt(1)
	v_mfma_f32_16x16x32_bf16 v[94:97], v[114:117], v[106:109], v[94:97]
	v_add_f32_e32 v114, v131, v118
	v_add_f32_e32 v114, v132, v114
	v_add_f32_e32 v203, v203, v114
	s_waitcnt lgkmcnt(0)
	v_mfma_f32_16x16x32_bf16 v[90:93], v[110:113], v[106:109], v[90:93]

; __device__ __forceinline__ float dpp_xor1(float v) { return __int_as_float(__builtin_amdgcn_update_dpp(0, __float_as_int(v), 0xB1, 0xf, 0xf, false)); }
;     ...
;                             if (__any(mx > mrun[qd] + 6.0f)) {
;                                 mx = fmaxf(mx, __shfl_xor(mx, 16)); mx = fmaxf(mx, __shfl_xor(mx, 32));
;                                 const float mn = fmaxf(mrun[qd], mx), corr = __expf(mrun[qd] - mn); mrun[qd] = mn;
;                                 lrun[qd] *= corr;
; #pragma unroll
;                                 for (int dt = 0; dt < 4; ++dt) O[qd][dt] = O[qd][dt] * corr;
;                             }
;                             float negm = (mrun[qd] < -1e29f ? 0.f : -mrun[qd] * L2E) + boff; float ps = 0.f;
;                             if (MODE == 3 && !colsel) negm = -__builtin_inff();
; #pragma unroll
;                             for (int kt = 0; kt < 4; ++kt)
; #pragma unroll
;                                 for (int r = 0; r < 4; ++r) { p[kt][r] = (DBG == 2) ? sc[kt][r] + negm : __builtin_amdgcn_exp2f(__builtin_fmaf(sc[kt][r], L2E, negm)); ps += p[kt][r]; }
;                             lrun[qd] += ps;
;                         }
;                         if (MODE == 2 && pass == 1) {
;                             float base[4], im3[4], rot[4];
; #pragma unroll
;                             for (int kt = 0; kt < 4; ++kt) { float im[4];
; #pragma unroll
;                                 for (int r = 0; r < 4; ++r) { float v = p[kt][r]; v += dpp_xor1(v); v += dpp_xor2(v); im[r] = v; }
;                                 base[kt] = 2.0f * (im[0] + im[1] + im[2]) + im[3]; im3[kt] = im[3]; }
; #pragma unroll
;                             for (int kt = 0; kt < 4; ++kt) rot[kt] = __shfl(im3[kt], (lane + 48) & 63);
; #pragma unroll
;                             for (int kt = 0; kt < 4; ++kt) { const float pv3 = q > 0 ? rot[kt] : (kt == 0 ? carry3[qd] : rot[kt > 0 ? kt - 1 : 0]);
;                                 const int jg = (p0 + 16 * kt + 4 * q) >> 2;
;                                 if (hr == 0 && jg < 256) sscore[(tq - t0) * SSTR + jg] = base[kt] + pv3; }
;                             carry3[qd] = rot[3];
;                         }
;                         if (do_pv && DBG != 1) {
; #pragma unroll
;                             for (int st = 0; st < 2; ++st) {
.LBB0_1260:
	v_and_b32_e32 v192, s0, v205
	v_cmp_eq_u32_e64 s[0:1], 0, v192
	v_max3_f32 v192, v150, v151, v152
	v_max3_f32 v192, v192, v153, v146
	v_max3_f32 v192, v192, v147, v148
	v_max3_f32 v192, v192, v149, v142
	v_max3_f32 v192, v192, v143, v144
	v_max3_f32 v192, v192, v145, v106
	v_max3_f32 v192, v192, v107, v108
	v_max_f32_e32 v192, v192, v109
	v_add_f32_e32 v192, v237, v192
	v_cndmask_b32_e64 v192, v192, v190, s[0:1]
	v_add_f32_e32 v193, 0x40c00000, v236
	v_cmp_gt_f32_e32 vcc, v192, v193
	s_cbranch_vccz .LBB0_1262
	ds_bpermute_b32 v193, v230, v192
	v_max_f32_e32 v192, v192, v192
	s_waitcnt lgkmcnt(0)
	v_max_f32_e32 v193, v193, v193
	v_max_f32_e32 v192, v192, v193
	ds_bpermute_b32 v193, v231, v192
	s_waitcnt lgkmcnt(0)
	v_max3_f32 v193, v236, v192, v193
	v_sub_f32_e32 v192, v236, v193
	v_mul_f32_e32 v192, 0x3fb8aa3b, v192
	v_exp_f32_e32 v192, v192
	v_mov_b32_e32 v236, v193
	v_mul_f32_e32 v202, v202, v192
	v_pk_mul_f32 v[88:89], v[88:89], v[192:193] op_sel_hi:[1,0]
	v_pk_mul_f32 v[86:87], v[86:87], v[192:193] op_sel_hi:[1,0]
	v_pk_mul_f32 v[84:85], v[84:85], v[192:193] op_sel_hi:[1,0]
	v_pk_mul_f32 v[82:83], v[82:83], v[192:193] op_sel_hi:[1,0]
	v_pk_mul_f32 v[80:81], v[80:81], v[192:193] op_sel_hi:[1,0]
	v_pk_mul_f32 v[78:79], v[78:79], v[192:193] op_sel_hi:[1,0]
	v_pk_mul_f32 v[76:77], v[76:77], v[192:193] op_sel_hi:[1,0]
	v_pk_mul_f32 v[74:75], v[74:75], v[192:193] op_sel_hi:[1,0]
	v_mul_f32_e32 v250, 0xbfb8aa3b, v193
	v_cmp_ngt_f32_e32 vcc, s30, v193
	s_nop 1
	v_cndmask_b32_e32 v250, 0, v250, vcc
.LBB0_1262:
	v_fmamk_f32 v192, v237, 0x3fb8aa3b, v250
	v_cndmask_b32_e64 v192, v192, v194, s[0:1]
	v_fmamk_f32 v150, v150, 0x3fb8aa3b, v192
	v_fmamk_f32 v151, v151, 0x3fb8aa3b, v192
	v_fmamk_f32 v152, v152, 0x3fb8aa3b, v192
	v_fmamk_f32 v153, v153, 0x3fb8aa3b, v192
	v_fmamk_f32 v146, v146, 0x3fb8aa3b, v192
	v_fmamk_f32 v147, v147, 0x3fb8aa3b, v192
	v_fmamk_f32 v148, v148, 0x3fb8aa3b, v192
	v_fmamk_f32 v149, v149, 0x3fb8aa3b, v192
	v_exp_f32_e32 v150, v150
	v_exp_f32_e32 v151, v151
	v_exp_f32_e32 v152, v152
	v_exp_f32_e32 v153, v153
	v_exp_f32_e32 v146, v146
	v_exp_f32_e32 v147, v147
	v_exp_f32_e32 v148, v148
	v_exp_f32_e32 v149, v149
	v_fmamk_f32 v142, v142, 0x3fb8aa3b, v192
	v_exp_f32_e32 v237, v142
	v_fmamk_f32 v142, v143, 0x3fb8aa3b, v192
	v_exp_f32_e32 v238, v142
	v_fmamk_f32 v142, v144, 0x3fb8aa3b, v192
	v_add_f32_e32 v193, 0, v150
	v_exp_f32_e32 v239, v142
	v_fmamk_f32 v240, v145, 0x3fb8aa3b, v192
	v_cvt_pk_bf16_f32 v142, v150, v151
	v_cvt_pk_bf16_f32 v143, v152, v153
	v_cvt_pk_bf16_f32 v144, v146, v147
	v_cvt_pk_bf16_f32 v145, v148, v149
	v_fmamk_f32 v106, v106, 0x3fb8aa3b, v192
	v_add_f32_e32 v193, v151, v193
	s_waitcnt lgkmcnt(7)
	v_mfma_f32_16x16x32_bf16 v[86:89], v[138:141], v[142:145], v[86:89]
	v_exp_f32_e32 v139, v106
	v_fmamk_f32 v106, v107, 0x3fb8aa3b, v192
	v_add_f32_e32 v193, v152, v193
	s_waitcnt lgkmcnt(6)
	v_mfma_f32_16x16x32_bf16 v[82:85], v[130:133], v[142:145], v[82:85]
	v_exp_f32_e32 v130, v106
	v_fmamk_f32 v106, v108, 0x3fb8aa3b, v192
	v_fmac_f32_e32 v192, 0x3fb8aa3b, v109
	v_add_f32_e32 v193, v153, v193
	v_exp_f32_e32 v138, v240
	v_exp_f32_e32 v131, v106
	v_exp_f32_e32 v132, v192
	v_add_f32_e32 v193, v146, v193
	v_add_f32_e32 v193, v147, v193
	v_add_f32_e32 v193, v148, v193
	v_add_f32_e32 v193, v149, v193
	v_cvt_pk_bf16_f32 v106, v237, v238
	v_cvt_pk_bf16_f32 v107, v239, v138
	v_cvt_pk_bf16_f32 v108, v139, v130
	v_cvt_pk_bf16_f32 v109, v131, v132
	s_waitcnt lgkmcnt(5)
	v_mfma_f32_16x16x32_bf16 v[78:81], v[134:137], v[142:145], v[78:81]
	s_waitcnt lgkmcnt(3)
	v_mfma_f32_16x16x32_bf16 v[86:89], v[122:125], v[106:109], v[86:89]
	v_add_f32_e32 v122, v237, v193
	v_add_f32_e32 v122, v238, v122
	v_add_f32_e32 v122, v239, v122
	v_mfma_f32_16x16x32_bf16 v[74:77], v[126:129], v[142:145], v[74:77]
	s_waitcnt lgkmcnt(2)
	v_mfma_f32_16x16x32_bf16 v[82:85], v[118:121], v[106:109], v[82:85]
	v_add_f32_e32 v118, v138, v122
	v_add_f32_e32 v118, v139, v118
	v_add_f32_e32 v118, v130, v118
	s_waitcnt lgkmcnt(1)
	v_mfma_f32_16x16x32_bf16 v[78:81], v[114:117], v[106:109], v[78:81]
	v_add_f32_e32 v114, v131, v118
	v_add_f32_e32 v114, v132, v114
	v_add_f32_e32 v202, v202, v114
	s_waitcnt lgkmcnt(0)
	v_mfma_f32_16x16x32_bf16 v[74:77], v[110:113], v[106:109], v[74:77]
